# v032 + epilogue: one merged vmcnt wait per store group
# baseline (speedup 1.0000x reference)
.LBB3_141:
	s_mul_i32 s2, s41, 0x6000
	v_or_b32_e32 v98, s2, v206
	v_add_u32_e32 v250, 0x12000, v98
	ds_read_b128 v[98:101], v250 offset:8192
	v_cvt_pk_bf16_f32 v50, v50, v51
	v_cvt_pk_bf16_f32 v51, v52, v53
	v_cvt_pk_bf16_f32 v52, v54, v55
	v_cvt_pk_bf16_f32 v53, v56, v57
	ds_read_b128 v[54:57], v250 offset:9216
	v_cvt_pk_bf16_f32 v214, v82, v83
	v_cvt_pk_bf16_f32 v215, v84, v85
	ds_read_b128 v[82:85], v250 offset:13312
	s_waitcnt lgkmcnt(2)
	v_mfma_f32_32x32x16_bf16 v[114:129], v[98:101], v[50:53], 0
	ds_read_b128 v[98:101], v250 offset:12288
	v_cvt_pk_bf16_f32 v18, v18, v19
	v_cvt_pk_bf16_f32 v19, v20, v21
	v_cvt_pk_bf16_f32 v20, v22, v23
	v_cvt_pk_bf16_f32 v21, v24, v25
	v_cvt_pk_bf16_f32 v216, v86, v87
	v_cvt_pk_bf16_f32 v217, v88, v89
	v_cvt_pk_bf16_f32 v86, v10, v11
	s_waitcnt lgkmcnt(0)
	v_mfma_f32_32x32x16_bf16 v[98:113], v[98:101], v[50:53], 0
	v_cvt_pk_bf16_f32 v50, v58, v59
	v_cvt_pk_bf16_f32 v51, v60, v61
	v_cvt_pk_bf16_f32 v52, v62, v63
	v_cvt_pk_bf16_f32 v53, v64, v65
	ds_read_b128 v[58:61], v250 offset:10240
	v_cvt_pk_bf16_f32 v87, v12, v13
	v_cvt_pk_bf16_f32 v88, v14, v15
	v_mfma_f32_32x32x16_bf16 v[114:129], v[54:57], v[50:53], v[114:129]
	v_cvt_pk_bf16_f32 v2, v2, v3
	v_cvt_pk_bf16_f32 v3, v4, v5
	v_cvt_pk_bf16_f32 v4, v6, v7
	v_cvt_pk_bf16_f32 v5, v8, v9
	v_cvt_pk_bf16_f32 v6, v42, v43
	v_cvt_pk_bf16_f32 v7, v44, v45
	v_cvt_pk_bf16_f32 v8, v46, v47
	v_mfma_f32_32x32x16_bf16 v[98:113], v[82:85], v[50:53], v[98:113]
	ds_read_b128 v[22:25], v250 offset:14336
	ds_read_b128 v[50:53], v250 offset:11264
	ds_read_b128 v[10:13], v250
	v_cvt_pk_bf16_f32 v9, v48, v49
	v_cvt_pk_bf16_f32 v54, v90, v91
	v_cvt_pk_bf16_f32 v55, v92, v93
	v_cvt_pk_bf16_f32 v56, v94, v95
	v_cvt_pk_bf16_f32 v57, v96, v97
	s_waitcnt lgkmcnt(3)
	v_mfma_f32_32x32x16_bf16 v[114:129], v[58:61], v[18:21], v[114:129]
	v_cvt_pk_bf16_f32 v58, v34, v35
	v_cvt_pk_bf16_f32 v59, v36, v37
	ds_read_b128 v[34:37], v250 offset:15360
	v_cvt_pk_bf16_f32 v60, v38, v39
	v_cvt_pk_bf16_f32 v61, v40, v41
	v_cvt_pk_bf16_f32 v202, v66, v67
	v_cvt_pk_bf16_f32 v203, v68, v69
	s_waitcnt lgkmcnt(3)
	v_mfma_f32_32x32x16_bf16 v[98:113], v[22:25], v[18:21], v[98:113]
	v_cvt_pk_bf16_f32 v18, v26, v27
	v_cvt_pk_bf16_f32 v19, v28, v29
	v_cvt_pk_bf16_f32 v20, v30, v31
	v_cvt_pk_bf16_f32 v21, v32, v33
	v_cvt_pk_bf16_f32 v204, v70, v71
	v_cvt_pk_bf16_f32 v205, v72, v73
	v_cvt_pk_bf16_f32 v82, v74, v75
	s_waitcnt lgkmcnt(2)
	v_mfma_f32_32x32x16_bf16 v[114:129], v[50:53], v[18:21], v[114:129]
	v_cvt_pk_bf16_f32 v83, v76, v77
	v_cvt_pk_bf16_f32 v84, v78, v79
	v_cvt_pk_bf16_f32 v85, v80, v81
	s_lshl_b32 s2, s20, 6
	s_mov_b32 s41, 1
	s_mov_b64 s[20:21], 0
	s_nop 5
	v_max3_f32 v14, v114, s38, v115
	s_waitcnt lgkmcnt(0)
	v_mfma_f32_32x32x16_bf16 v[98:113], v[34:37], v[18:21], v[98:113]
	ds_read_b128 v[50:53], v250 offset:1024
	ds_read_b128 v[18:21], v250 offset:4096
	ds_read_b128 v[62:65], v250 offset:5120
	v_max3_f32 v14, v14, v116, v117
	v_max3_f32 v14, v14, v118, v119
	v_max3_f32 v14, v14, v120, v121
	v_max3_f32 v14, v14, v122, v123
	v_max3_f32 v14, v14, v124, v125
	v_max3_f32 v14, v14, v126, v127
	v_mfma_f32_32x32x16_bf16 v[34:49], v[214:217], v[10:13], 0
	v_max3_f32 v14, v14, v128, v129
	s_nop 0
	v_max3_f32 v14, v14, v98, v99
	v_max3_f32 v14, v14, v100, v101
	v_max3_f32 v14, v14, v102, v103
	v_max3_f32 v14, v14, v104, v105
	v_max3_f32 v14, v14, v106, v107
	v_max3_f32 v14, v14, v108, v109
	s_waitcnt lgkmcnt(1)
	v_mfma_f32_32x32x16_bf16 v[18:33], v[214:217], v[18:21], 0
	v_max3_f32 v14, v14, v110, v111
	v_max3_f32 v14, v14, v112, v113
	v_mov_b32_e32 v15, v14
	ds_read_b128 v[10:13], v250 offset:2048
	ds_read_b128 v[66:69], v250 offset:3072
	ds_read_b128 v[70:73], v250 offset:6144
	ds_read_b128 v[74:77], v250 offset:7168
	v_permlane32_swap_b32_e32 v14, v15
	v_max_f32_e32 v15, v15, v15
	v_mfma_f32_32x32x16_bf16 v[34:49], v[54:57], v[50:53], v[34:49]
	v_max_f32_e32 v14, v14, v14
	v_max_f32_e32 v14, v14, v15
	v_mul_f32_e32 v14, 0xbe38aa3b, v14
	v_fmamk_f32 v15, v114, 0x3e38aa3b, v14
	v_fmamk_f32 v50, v118, 0x3e38aa3b, v14
	v_exp_f32_e32 v50, v50
	v_fmamk_f32 v51, v119, 0x3e38aa3b, v14
	s_waitcnt lgkmcnt(4)
	v_mfma_f32_32x32x16_bf16 v[18:33], v[54:57], v[62:65], v[18:33]
	v_exp_f32_e32 v51, v51
	v_fmamk_f32 v52, v120, 0x3e38aa3b, v14
	v_exp_f32_e32 v52, v52
	v_fmamk_f32 v53, v121, 0x3e38aa3b, v14
	v_exp_f32_e32 v53, v53
	v_fmamk_f32 v109, v109, 0x3e38aa3b, v14
	s_waitcnt lgkmcnt(3)
	v_mfma_f32_32x32x16_bf16 v[34:49], v[58:61], v[10:13], v[34:49]
	v_exp_f32_e32 v10, v15
	v_fmamk_f32 v11, v115, 0x3e38aa3b, v14
	v_exp_f32_e32 v11, v11
	v_fmamk_f32 v12, v116, 0x3e38aa3b, v14
	v_exp_f32_e32 v12, v12
	v_fmamk_f32 v15, v117, 0x3e38aa3b, v14
	v_exp_f32_e32 v15, v15
	s_waitcnt lgkmcnt(1)
	v_mfma_f32_32x32x16_bf16 v[18:33], v[58:61], v[70:73], v[18:33]
	v_add_f32_e32 v13, 0, v10
	v_add_f32_e32 v13, v13, v11
	v_add_f32_e32 v13, v13, v12
	v_add_f32_e32 v13, v13, v15
	v_add_f32_e32 v13, v13, v50
	v_add_f32_e32 v13, v13, v51
	v_cvt_pk_bf16_f32 v10, v10, v11
	v_mfma_f32_32x32x16_bf16 v[34:49], v[6:9], v[66:69], v[34:49]
	v_cvt_pk_bf16_f32 v11, v12, v15
	v_cvt_pk_bf16_f32 v12, v50, v51
	s_waitcnt lgkmcnt(0)
	v_mfma_f32_32x32x16_bf16 v[18:33], v[6:9], v[74:77], v[18:33]
	v_fmamk_f32 v6, v122, 0x3e38aa3b, v14
	v_exp_f32_e32 v89, v6
	v_fmamk_f32 v6, v123, 0x3e38aa3b, v14
	v_exp_f32_e32 v94, v6
	v_fmamk_f32 v7, v124, 0x3e38aa3b, v14
	v_add_f32_e32 v6, v13, v52
	v_exp_f32_e32 v95, v7
	v_fmamk_f32 v7, v125, 0x3e38aa3b, v14
	v_add_f32_e32 v6, v6, v53
	v_exp_f32_e32 v96, v7
	v_fmamk_f32 v7, v126, 0x3e38aa3b, v14
	v_add_f32_e32 v6, v6, v89
	v_exp_f32_e32 v97, v7
	v_fmamk_f32 v7, v127, 0x3e38aa3b, v14
	v_add_f32_e32 v6, v6, v94
	v_exp_f32_e32 v114, v7
	v_fmamk_f32 v7, v128, 0x3e38aa3b, v14
	v_add_f32_e32 v6, v6, v95
	v_exp_f32_e32 v115, v7
	v_fmamk_f32 v7, v129, 0x3e38aa3b, v14
	v_add_f32_e32 v6, v6, v96
	v_exp_f32_e32 v116, v7
	v_fmamk_f32 v7, v98, 0x3e38aa3b, v14
	v_add_f32_e32 v6, v6, v97
	v_exp_f32_e32 v98, v7
	v_fmamk_f32 v7, v99, 0x3e38aa3b, v14
	v_add_f32_e32 v6, v6, v114
	v_exp_f32_e32 v99, v7
	v_fmamk_f32 v7, v100, 0x3e38aa3b, v14
	v_add_f32_e32 v6, v6, v115
	v_exp_f32_e32 v100, v7
	v_fmamk_f32 v7, v101, 0x3e38aa3b, v14
	v_add_f32_e32 v6, v6, v116
	v_exp_f32_e32 v101, v7
	v_fmamk_f32 v7, v102, 0x3e38aa3b, v14
	v_add_f32_e32 v6, v6, v98
	v_exp_f32_e32 v102, v7
	v_fmamk_f32 v7, v103, 0x3e38aa3b, v14
	v_add_f32_e32 v6, v6, v99
	v_exp_f32_e32 v103, v7
	v_add_f32_e32 v6, v6, v100
	v_add_f32_e32 v6, v6, v101
	v_add_f32_e32 v6, v6, v102
	v_add_f32_e32 v54, v6, v103
	v_fmamk_f32 v6, v104, 0x3e38aa3b, v14
	v_exp_f32_e32 v104, v6
	ds_read_b128 v[6:9], v250 offset:16384
	v_fmamk_f32 v13, v105, 0x3e38aa3b, v14
	v_exp_f32_e32 v105, v13
	v_cvt_pk_bf16_f32 v13, v52, v53
	ds_read_b128 v[50:53], v250 offset:18432
	ds_read_b128 v[90:93], v250 offset:17408
	s_waitcnt lgkmcnt(2)
	v_mfma_f32_32x32x16_bf16 v[66:81], v[6:9], v[10:13], 0
	v_add_f32_e32 v6, v54, v104
	v_add_f32_e32 v15, v6, v105
	v_fmamk_f32 v6, v106, 0x3e38aa3b, v14
	v_exp_f32_e32 v106, v6
	v_fmamk_f32 v6, v107, 0x3e38aa3b, v14
	v_exp_f32_e32 v107, v6
	ds_read_b128 v[6:9], v250 offset:19456
	s_waitcnt lgkmcnt(2)
	v_mfma_f32_32x32x16_bf16 v[50:65], v[50:53], v[10:13], 0
	v_fmamk_f32 v10, v108, 0x3e38aa3b, v14
	v_exp_f32_e32 v108, v10
	v_cvt_pk_bf16_f32 v10, v89, v94
	v_cvt_pk_bf16_f32 v11, v95, v96
	v_cvt_pk_bf16_f32 v12, v97, v114
	v_cvt_pk_bf16_f32 v13, v115, v116
	v_fmamk_f32 v94, v110, 0x3e38aa3b, v14
	v_exp_f32_e32 v89, v109
	s_waitcnt lgkmcnt(1)
	v_mfma_f32_32x32x16_bf16 v[66:81], v[90:93], v[10:13], v[66:81]
	ds_read_b128 v[90:93], v250 offset:20480
	v_exp_f32_e32 v109, v94
	v_add_f32_e32 v15, v15, v106
	v_add_f32_e32 v15, v15, v107
	v_add_f32_e32 v15, v15, v108
	v_add_f32_e32 v15, v15, v89
	v_add_f32_e32 v15, v15, v109
	s_waitcnt lgkmcnt(1)
	v_mfma_f32_32x32x16_bf16 v[50:65], v[6:9], v[10:13], v[50:65]
	v_cvt_pk_bf16_f32 v6, v98, v99
	v_cvt_pk_bf16_f32 v7, v100, v101
	v_cvt_pk_bf16_f32 v8, v102, v103
	v_cvt_pk_bf16_f32 v9, v104, v105
	ds_read_b128 v[10:13], v250 offset:22528
	ds_read_b128 v[94:97], v250 offset:21504
	s_waitcnt lgkmcnt(2)
	v_mfma_f32_32x32x16_bf16 v[66:81], v[90:93], v[6:9], v[66:81]
	v_fmamk_f32 v90, v111, 0x3e38aa3b, v14
	v_exp_f32_e32 v98, v90
	v_fmamk_f32 v90, v112, 0x3e38aa3b, v14
	v_fmac_f32_e32 v14, 0x3e38aa3b, v113
	v_exp_f32_e32 v99, v90
	ds_read_b128 v[90:93], v250 offset:23552
	v_add_f32_e32 v15, v15, v98
	s_waitcnt lgkmcnt(2)
	v_mfma_f32_32x32x16_bf16 v[50:65], v[10:13], v[6:9], v[50:65]
	v_exp_f32_e32 v11, v14
	v_add_f32_e32 v10, v15, v99
	v_cvt_pk_bf16_f32 v6, v106, v107
	v_cvt_pk_bf16_f32 v7, v108, v89
	v_cvt_pk_bf16_f32 v8, v109, v98
	v_cvt_pk_bf16_f32 v9, v99, v11
	v_add_f32_e32 v10, v10, v11
	v_mov_b32_e32 v11, v10
	s_waitcnt lgkmcnt(1)
	v_mfma_f32_32x32x16_bf16 v[66:81], v[94:97], v[6:9], v[66:81]
	v_permlane32_swap_b32_e32 v10, v11
	v_add_f32_e32 v10, v10, v11
	v_rcp_f32_e32 v101, v10
	v_cvt_pk_bf16_f32 v89, v16, v17
	v_ashrrev_i32_e32 v118, 3, v210
	v_and_b32_e32 v118, 0xffffffe0, v118
	v_bfe_u32 v119, v210, 6, 1
	v_add_u32_e32 v118, s16, v118
	v_lshl_or_b32 v118, v119, 4, v118
	v_or_b32_e32 v118, v118, v211
	v_lshlrev_b32_e32 v118, 10, v118
	v_add_u32_e32 v118, s2, v118
	v_bfe_u32 v119, v210, 7, 1
	v_lshl_or_b32 v118, v119, 5, v118
	v_or_b32_e32 v118, v118, v1
	v_lshlrev_b32_e32 v118, 2, v118
	global_load_dword v110, v118, s[12:13]
	global_load_dword v111, v118, s[72:73] offset:-4096
	global_load_dword v112, v118, s[72:73]
	global_load_dword v113, v118, s[76:77] offset:-4096
	global_load_dword v114, v118, s[76:77]
	global_load_dword v115, v118, s[78:79] offset:-4096
	global_load_dword v116, v118, s[78:79]
	global_load_dword v117, v118, s[74:75]
	s_nop 6
	s_waitcnt vmcnt(32)
	v_fmac_f32_e32 v245, v101, v70
	s_waitcnt lgkmcnt(0)
	v_mfma_f32_32x32x16_bf16 v[50:65], v[90:93], v[6:9], v[50:65]
	v_fmac_f32_e32 v243, v101, v71
	v_fmac_f32_e32 v241, v101, v72
	v_fmac_f32_e32 v239, v101, v73
	global_store_dword v252, v245, s[58:59] nt
	global_store_dword v252, v243, s[58:59] offset:1024 nt
	global_store_dword v252, v241, s[58:59] offset:2048 nt
	global_store_dword v252, v239, s[58:59] offset:3072 nt
	v_max3_f32 v6, v34, s38, v35
	v_max3_f32 v6, v6, v36, v37
	v_max3_f32 v6, v6, v38, v39
	v_max3_f32 v6, v6, v40, v41
	v_max3_f32 v7, v18, s38, v19
	v_max3_f32 v6, v6, v42, v43
	v_max3_f32 v7, v7, v20, v21
	v_max3_f32 v6, v6, v44, v45
	v_max3_f32 v7, v7, v22, v23
	v_max3_f32 v6, v6, v46, v47
	v_max3_f32 v7, v7, v24, v25
	v_max3_f32 v6, v6, v48, v49
	v_max3_f32 v7, v7, v26, v27
	v_max3_f32 v7, v7, v28, v29
	v_mov_b32_e32 v8, v6
	s_waitcnt vmcnt(32)
	v_fmac_f32_e32 v244, v101, v74
	v_fmac_f32_e32 v242, v101, v75
	v_fmac_f32_e32 v240, v101, v76
	v_fmac_f32_e32 v238, v101, v77
	global_store_dword v252, v244, s[60:61] nt
	global_store_dword v252, v242, s[60:61] offset:1024 nt
	global_store_dword v252, v240, s[60:61] offset:2048 nt
	global_store_dword v252, v238, s[60:61] offset:3072 nt
	v_max3_f32 v7, v7, v30, v31
	s_nop 0
	v_permlane32_swap_b32_e32 v6, v8
	v_max3_f32 v7, v7, v32, v33
	v_max_f32_e32 v8, v8, v8
	v_max_f32_e32 v6, v6, v6
	v_max_f32_e32 v90, v6, v8
	v_mov_b32_e32 v6, v7
	s_nop 1
	v_permlane32_swap_b32_e32 v7, v6
	v_mul_f32_e32 v8, 0xbe38aa3b, v90
	v_fmamk_f32 v9, v34, 0x3e38aa3b, v8
	v_max_f32_e32 v6, v6, v6
	v_max_f32_e32 v7, v7, v7
	v_exp_f32_e32 v9, v9
	s_waitcnt vmcnt(30)
	v_fmac_f32_e32 v236, v101, v78
	v_fmac_f32_e32 v234, v101, v79
	v_fmac_f32_e32 v232, v101, v80
	v_fmac_f32_e32 v230, v101, v81
	global_store_dword v252, v236, s[62:63] nt
	global_store_dword v252, v234, s[62:63] offset:1024 nt
	global_store_dword v252, v232, s[62:63] offset:2048 nt
	global_store_dword v252, v230, s[62:63] offset:3072 nt
	v_max_f32_e32 v91, v7, v6
	v_fmamk_f32 v7, v35, 0x3e38aa3b, v8
	v_exp_f32_e32 v7, v7
	v_fmamk_f32 v10, v36, 0x3e38aa3b, v8
	v_exp_f32_e32 v10, v10
	v_fmamk_f32 v11, v37, 0x3e38aa3b, v8
	v_exp_f32_e32 v11, v11
	v_fmamk_f32 v12, v38, 0x3e38aa3b, v8
	v_add_f32_e32 v6, 0, v9
	v_exp_f32_e32 v12, v12
	v_fmamk_f32 v13, v39, 0x3e38aa3b, v8
	v_add_f32_e32 v6, v6, v7
	v_exp_f32_e32 v13, v13
	v_fmamk_f32 v14, v40, 0x3e38aa3b, v8
	v_add_f32_e32 v6, v6, v10
	s_waitcnt vmcnt(32)
	v_fmac_f32_e32 v237, v101, v50
	v_fmac_f32_e32 v235, v101, v51
	v_fmac_f32_e32 v233, v101, v52
	v_fmac_f32_e32 v231, v101, v53
	global_store_dword v252, v237, s[64:65] nt
	global_store_dword v252, v235, s[64:65] offset:1024 nt
	global_store_dword v252, v233, s[64:65] offset:2048 nt
	global_store_dword v252, v231, s[64:65] offset:3072 nt
	v_exp_f32_e32 v14, v14
	v_fmamk_f32 v15, v41, 0x3e38aa3b, v8
	v_fmamk_f32 v16, v42, 0x3e38aa3b, v8
	v_add_f32_e32 v6, v6, v11
	v_exp_f32_e32 v15, v15
	v_exp_f32_e32 v92, v16
	v_fmamk_f32 v16, v43, 0x3e38aa3b, v8
	v_add_f32_e32 v6, v6, v12
	v_exp_f32_e32 v93, v16
	v_fmamk_f32 v16, v44, 0x3e38aa3b, v8
	v_add_f32_e32 v6, v6, v13
	v_exp_f32_e32 v94, v16
	v_fmamk_f32 v16, v45, 0x3e38aa3b, v8
	v_add_f32_e32 v6, v6, v14
	v_exp_f32_e32 v95, v16
	s_waitcnt vmcnt(32)
	v_fmac_f32_e32 v228, v101, v54
	v_fmac_f32_e32 v226, v101, v55
	v_fmac_f32_e32 v224, v101, v56
	v_fmac_f32_e32 v222, v101, v57
	global_store_dword v252, v228, s[66:67] nt
	global_store_dword v252, v226, s[66:67] offset:1024 nt
	global_store_dword v252, v224, s[66:67] offset:2048 nt
	global_store_dword v252, v222, s[66:67] offset:3072 nt
	v_fmamk_f32 v16, v46, 0x3e38aa3b, v8
	v_add_f32_e32 v6, v6, v15
	v_exp_f32_e32 v96, v16
	v_fmamk_f32 v16, v47, 0x3e38aa3b, v8
	v_add_f32_e32 v6, v6, v92
	v_exp_f32_e32 v97, v16
	v_fmamk_f32 v16, v48, 0x3e38aa3b, v8
	v_add_f32_e32 v6, v6, v93
	v_exp_f32_e32 v98, v16
	v_fmac_f32_e32 v8, 0x3e38aa3b, v49
	v_mul_f32_e32 v16, 0xbe38aa3b, v91
	v_add_f32_e32 v6, v6, v94
	v_exp_f32_e32 v99, v8
	v_fmamk_f32 v8, v18, 0x3e38aa3b, v16
	v_add_f32_e32 v6, v6, v95
	v_fmac_f32_e32 v249, v101, v66
	v_fmac_f32_e32 v248, v101, v67
	v_fmac_f32_e32 v247, v101, v68
	v_fmac_f32_e32 v246, v101, v69
	global_store_dword v252, v249, s[4:5] nt
	global_store_dword v252, v248, s[4:5] offset:1024 nt
	global_store_dword v252, v247, s[4:5] offset:2048 nt
	global_store_dword v252, v246, s[4:5] offset:3072 nt
	v_exp_f32_e32 v17, v8
	v_fmamk_f32 v8, v19, 0x3e38aa3b, v16
	v_add_f32_e32 v6, v6, v96
	v_exp_f32_e32 v18, v8
	v_fmamk_f32 v8, v20, 0x3e38aa3b, v16
	v_add_f32_e32 v6, v6, v97
	v_exp_f32_e32 v19, v8
	v_fmamk_f32 v8, v21, 0x3e38aa3b, v16
	v_add_f32_e32 v6, v6, v98
	v_exp_f32_e32 v20, v8
	v_fmamk_f32 v8, v22, 0x3e38aa3b, v16
	v_add_f32_e32 v100, v6, v99
	v_add_f32_e32 v6, 0, v17
	v_exp_f32_e32 v21, v8
	s_waitcnt vmcnt(32)
	v_fmac_f32_e32 v221, v101, v62
	v_fmac_f32_e32 v220, v101, v63
	v_fmac_f32_e32 v219, v101, v64
	v_fmac_f32_e32 v218, v101, v65
	global_store_dword v252, v221, s[70:71] nt
	global_store_dword v252, v220, s[70:71] offset:1024 nt
	global_store_dword v252, v219, s[70:71] offset:2048 nt
	global_store_dword v252, v218, s[70:71] offset:3072 nt
	v_fmamk_f32 v8, v23, 0x3e38aa3b, v16
	v_add_f32_e32 v6, v6, v18
	v_exp_f32_e32 v22, v8
	v_fmamk_f32 v8, v24, 0x3e38aa3b, v16
	v_add_f32_e32 v6, v6, v19
	v_exp_f32_e32 v23, v8
	v_fmamk_f32 v8, v25, 0x3e38aa3b, v16
	v_add_f32_e32 v6, v6, v20
	v_exp_f32_e32 v24, v8
	v_fmamk_f32 v8, v26, 0x3e38aa3b, v16
	v_add_f32_e32 v6, v6, v21
	v_exp_f32_e32 v25, v8
	v_add_f32_e32 v6, v6, v22
	v_add_f32_e32 v6, v6, v23
	v_fmac_f32_e32 v229, v101, v58
	v_fmac_f32_e32 v227, v101, v59
	v_fmac_f32_e32 v225, v101, v60
	v_fmac_f32_e32 v223, v101, v61
	global_store_dword v252, v229, s[68:69] nt
	global_store_dword v252, v227, s[68:69] offset:1024 nt
	global_store_dword v252, v225, s[68:69] offset:2048 nt
	global_store_dword v252, v223, s[68:69] offset:3072 nt
	v_add_f32_e32 v6, v6, v24
	v_add_f32_e32 v26, v6, v25
	v_fmamk_f32 v6, v27, 0x3e38aa3b, v16
	v_exp_f32_e32 v27, v6
	v_cvt_pk_bf16_f32 v6, v9, v7
	v_cvt_pk_bf16_f32 v7, v10, v11
	v_fmamk_f32 v10, v28, 0x3e38aa3b, v16
	v_cvt_pk_bf16_f32 v9, v14, v15
	v_exp_f32_e32 v28, v10
	v_fmamk_f32 v14, v29, 0x3e38aa3b, v16
	v_cvt_pk_bf16_f32 v8, v12, v13
	v_cvt_pk_bf16_f32 v13, v23, v24
	v_exp_f32_e32 v23, v14
	v_fmamk_f32 v14, v30, 0x3e38aa3b, v16
	v_mfma_f32_32x32x16_bf16 v[66:81], v[202:205], v[6:9], 0
	v_exp_f32_e32 v24, v14
	v_add_f32_e32 v14, v26, v27
	v_add_f32_e32 v14, v14, v28
	v_add_f32_e32 v14, v14, v23
	v_cvt_pk_bf16_f32 v10, v17, v18
	v_cvt_pk_bf16_f32 v11, v19, v20
	v_cvt_pk_bf16_f32 v12, v21, v22
	v_mfma_f32_32x32x16_bf16 v[34:49], v[2:5], v[6:9], 0
	v_fmamk_f32 v6, v31, 0x3e38aa3b, v16
	v_exp_f32_e32 v26, v6
	v_add_f32_e32 v14, v14, v24
	v_fmamk_f32 v6, v32, 0x3e38aa3b, v16
	v_fmac_f32_e32 v16, 0x3e38aa3b, v33
	v_exp_f32_e32 v29, v6
	v_exp_f32_e32 v30, v16
	v_mfma_f32_32x32x16_bf16 v[50:65], v[202:205], v[10:13], 0
	v_add_f32_e32 v18, v14, v26
	v_mov_b32_e32 v22, v100
	s_nop 1
	v_permlane32_swap_b32_e32 v100, v22
	v_add_f32_e32 v32, v100, v22
	v_cvt_pk_bf16_f32 v22, v25, v27
	v_cvt_pk_bf16_f32 v23, v28, v23
	v_mfma_f32_32x32x16_bf16 v[2:17], v[2:5], v[10:13], 0
	v_cvt_pk_bf16_f32 v24, v24, v26
	v_cvt_pk_bf16_f32 v25, v29, v30
	v_lshlrev_b32_e32 v26, 2, v213
	v_lshl_or_b32 v27, v212, 10, v26
	v_add_f32_e32 v18, v18, v29
	v_add_u32_e32 v28, 0x10000, v27
	v_add_f32_e32 v31, v18, v30
	v_mfma_f32_32x32x16_bf16 v[2:17], v[86:89], v[22:25], v[2:17]
	ds_write_b32 v28, v90
	v_add_u32_e32 v28, 0x10100, v27
	v_cvt_pk_bf16_f32 v18, v92, v93
	v_cvt_pk_bf16_f32 v19, v94, v95
	v_cvt_pk_bf16_f32 v20, v96, v97
	v_cvt_pk_bf16_f32 v21, v98, v99
	ds_write_b32 v28, v32
	v_mov_b32_e32 v28, v31
	v_mfma_f32_32x32x16_bf16 v[66:81], v[82:85], v[18:21], v[66:81]
	s_nop 0
	v_permlane32_swap_b32_e32 v31, v28
	s_nop 0
	v_cvt_pk_bf16_f32 v2, v2, v3
	v_cvt_pk_bf16_f32 v3, v4, v5
	v_cvt_pk_bf16_f32 v4, v6, v7
	v_cvt_pk_bf16_f32 v5, v8, v9
	v_mfma_f32_32x32x16_bf16 v[34:49], v[86:89], v[18:21], v[34:49]
	v_add_u32_e32 v19, 0x10200, v27
	v_add_f32_e32 v18, v31, v28
	ds_write_b32 v19, v91
	v_add_u32_e32 v19, 0x10300, v27
	ds_write_b32 v19, v18
	v_cvt_pk_bf16_f32 v18, v66, v67
	v_cvt_pk_bf16_f32 v19, v68, v69
	v_mfma_f32_32x32x16_bf16 v[50:65], v[82:85], v[22:25], v[50:65]
	v_lshl_or_b32 v22, v212, 13, v206
	ds_write_b128 v22, v[2:5] offset:6144
	v_cvt_pk_bf16_f32 v2, v10, v11
	v_cvt_pk_bf16_f32 v3, v12, v13
	v_cvt_pk_bf16_f32 v4, v14, v15
	v_cvt_pk_bf16_f32 v5, v16, v17
	ds_write_b128 v22, v[2:5] offset:7168
	v_bfe_u32 v16, v210, 6, 1
	v_ashrrev_i32_e32 v14, 7, v210
	v_and_b32_e32 v15, 1, v14
	v_cvt_pk_bf16_f32 v20, v70, v71
	v_cvt_pk_bf16_f32 v21, v72, v73
	ds_write_b128 v22, v[18:21]
	v_cvt_pk_bf16_f32 v18, v74, v75
	v_cvt_pk_bf16_f32 v19, v76, v77
	v_cvt_pk_bf16_f32 v20, v78, v79
	v_cvt_pk_bf16_f32 v21, v80, v81
	ds_write_b128 v22, v[18:21] offset:1024
	v_cvt_pk_bf16_f32 v18, v50, v51
	v_cvt_pk_bf16_f32 v19, v52, v53
	v_cvt_pk_bf16_f32 v20, v54, v55
	v_cvt_pk_bf16_f32 v21, v56, v57
	ds_write_b128 v22, v[18:21] offset:2048
	v_cvt_pk_bf16_f32 v18, v58, v59
	v_cvt_pk_bf16_f32 v19, v60, v61
	v_cvt_pk_bf16_f32 v20, v62, v63
	v_cvt_pk_bf16_f32 v21, v64, v65
	ds_write_b128 v22, v[18:21] offset:3072
	v_cvt_pk_bf16_f32 v18, v34, v35
	v_cvt_pk_bf16_f32 v19, v36, v37
	v_cvt_pk_bf16_f32 v20, v38, v39
	v_cvt_pk_bf16_f32 v21, v40, v41
	ds_write_b128 v22, v[18:21] offset:4096
	v_cvt_pk_bf16_f32 v18, v42, v43
	v_cvt_pk_bf16_f32 v19, v44, v45
	v_cvt_pk_bf16_f32 v20, v46, v47
	v_cvt_pk_bf16_f32 v21, v48, v49
	ds_write_b128 v22, v[18:21] offset:5120
	v_lshl_or_b32 v4, v15, 9, v26
	v_or_b32_e32 v5, 0x10000, v4
	v_or_b32_e32 v12, 0x10d00, v4
	s_waitcnt lgkmcnt(0)
	s_barrier
	v_or_b32_e32 v6, 0x10100, v4
	v_or_b32_e32 v7, 0x10400, v4
	v_or_b32_e32 v8, 0x10500, v4
	v_or_b32_e32 v9, 0x10800, v4
	v_or_b32_e32 v10, 0x10900, v4
	v_or_b32_e32 v11, 0x10c00, v4
	ds_read_b32 v5, v5
	ds_read_b32 v13, v6
	ds_read_b32 v15, v7
	ds_read_b32 v24, v8
	ds_read_b32 v25, v9
	ds_read_b32 v26, v10
	ds_read_b32 v27, v11
	ds_read_b32 v12, v12
	v_or_b32_e32 v6, 0x11000, v4
	v_or_b32_e32 v7, 0x11100, v4
	v_or_b32_e32 v8, 0x11400, v4
	v_or_b32_e32 v9, 0x11500, v4
	v_or_b32_e32 v10, 0x11800, v4
	v_or_b32_e32 v11, 0x11900, v4
	v_or_b32_e32 v28, 0x11c00, v4
	v_or_b32_e32 v4, 0x11d00, v4
	ds_read_b32 v29, v6
	ds_read_b32 v30, v7
	ds_read_b32 v31, v8
	ds_read_b32 v32, v9
	ds_read_b32 v33, v10
	ds_read_b32 v34, v11
	ds_read_b32 v28, v28
	ds_read_b32 v35, v4
	s_waitcnt lgkmcnt(13)
	v_max_f32_e32 v4, v15, v15
	v_max_f32_e32 v6, v5, v5
	v_max_f32_e32 v4, v6, v4
	s_waitcnt lgkmcnt(9)
	v_max3_f32 v4, v4, v25, v27
	s_waitcnt lgkmcnt(5)
	v_max3_f32 v4, v4, v29, v31
	s_waitcnt lgkmcnt(1)
	v_max3_f32 v36, v4, v33, v28
	v_sub_f32_e32 v4, v5, v36
	v_mul_f32_e32 v4, 0x3e38aa3b, v4
	v_exp_f32_e32 v37, v4
	v_lshlrev_b32_e32 v4, 11, v14
	v_lshlrev_b32_e32 v5, 10, v16
	v_or3_b32 v14, v206, v4, v5
	ds_read_b128 v[4:7], v14
	ds_read_b128 v[8:11], v14 offset:8192
	v_fma_f32 v13, v13, v37, 0
	s_waitcnt lgkmcnt(1)
	v_lshlrev_b32_e32 v16, 16, v4
	v_and_b32_e32 v4, 0xffff0000, v4
	v_fma_f32 v38, v37, v4, 0
	v_lshlrev_b32_e32 v4, 16, v5
	v_fma_f32 v39, v37, v4, 0
	v_and_b32_e32 v4, 0xffff0000, v5
	v_sub_f32_e32 v5, v15, v36
	v_fma_f32 v40, v37, v4, 0
	v_lshlrev_b32_e32 v4, 16, v6
	v_mul_f32_e32 v5, 0x3e38aa3b, v5
	v_fma_f32 v41, v37, v4, 0
	v_and_b32_e32 v4, 0xffff0000, v6
	v_exp_f32_e32 v15, v5
	v_fma_f32 v42, v37, v4, 0
	v_lshlrev_b32_e32 v4, 16, v7
	v_fma_f32 v43, v37, v4, 0
	v_and_b32_e32 v4, 0xffff0000, v7
	v_fma_f32 v16, v37, v16, 0
	v_fma_f32 v37, v37, v4, 0
	s_waitcnt lgkmcnt(0)
	v_lshlrev_b32_e32 v4, 16, v8
	v_fmac_f32_e32 v16, v15, v4
	v_and_b32_e32 v4, 0xffff0000, v8
	v_fmac_f32_e32 v38, v15, v4
	v_lshlrev_b32_e32 v4, 16, v9
	v_fmac_f32_e32 v39, v15, v4
	v_and_b32_e32 v4, 0xffff0000, v9
	v_fmac_f32_e32 v40, v15, v4
	v_lshlrev_b32_e32 v4, 16, v10
	v_fmac_f32_e32 v41, v15, v4
	v_and_b32_e32 v4, 0xffff0000, v10
	v_fmac_f32_e32 v42, v15, v4
	v_lshlrev_b32_e32 v4, 16, v11
	v_fmac_f32_e32 v43, v15, v4
	v_sub_f32_e32 v4, v25, v36
	v_mul_f32_e32 v4, 0x3e38aa3b, v4
	v_fmac_f32_e32 v13, v24, v15
	v_exp_f32_e32 v24, v4
	ds_read_b128 v[4:7], v14 offset:16384
	v_and_b32_e32 v8, 0xffff0000, v11
	v_fmac_f32_e32 v37, v15, v8
	ds_read_b128 v[8:11], v14 offset:24576
	v_fmac_f32_e32 v13, v26, v24
	s_waitcnt lgkmcnt(1)
	v_lshlrev_b32_e32 v15, 16, v4
	v_and_b32_e32 v4, 0xffff0000, v4
	v_fmac_f32_e32 v38, v24, v4
	v_lshlrev_b32_e32 v4, 16, v5
	v_fmac_f32_e32 v39, v24, v4
	v_and_b32_e32 v4, 0xffff0000, v5
	v_sub_f32_e32 v5, v27, v36
	v_fmac_f32_e32 v40, v24, v4
	v_lshlrev_b32_e32 v4, 16, v6
	v_mul_f32_e32 v5, 0x3e38aa3b, v5
	v_fmac_f32_e32 v16, v24, v15
	v_fmac_f32_e32 v41, v24, v4
	v_and_b32_e32 v4, 0xffff0000, v6
	v_exp_f32_e32 v15, v5
	v_fmac_f32_e32 v42, v24, v4
	v_lshlrev_b32_e32 v4, 16, v7
	v_fmac_f32_e32 v43, v24, v4
	v_and_b32_e32 v4, 0xffff0000, v7
	v_fmac_f32_e32 v37, v24, v4
	s_waitcnt lgkmcnt(0)
	v_lshlrev_b32_e32 v4, 16, v8
	v_fmac_f32_e32 v16, v15, v4
	v_and_b32_e32 v4, 0xffff0000, v8
	v_fmac_f32_e32 v38, v15, v4
	v_lshlrev_b32_e32 v4, 16, v9
	v_fmac_f32_e32 v39, v15, v4
	v_and_b32_e32 v4, 0xffff0000, v9
	v_fmac_f32_e32 v40, v15, v4
	v_lshlrev_b32_e32 v4, 16, v10
	v_fmac_f32_e32 v41, v15, v4
	v_and_b32_e32 v4, 0xffff0000, v10
	v_fmac_f32_e32 v42, v15, v4
	v_lshlrev_b32_e32 v4, 16, v11
	v_fmac_f32_e32 v43, v15, v4
	v_sub_f32_e32 v4, v29, v36
	v_mul_f32_e32 v4, 0x3e38aa3b, v4
	v_fmac_f32_e32 v13, v12, v15
	v_exp_f32_e32 v12, v4
	ds_read_b128 v[4:7], v14 offset:32768
	v_and_b32_e32 v8, 0xffff0000, v11
	v_fmac_f32_e32 v37, v15, v8
	ds_read_b128 v[8:11], v14 offset:40960
	v_fmac_f32_e32 v13, v30, v12
	s_waitcnt lgkmcnt(1)
	v_lshlrev_b32_e32 v15, 16, v4
	v_and_b32_e32 v4, 0xffff0000, v4
	v_fmac_f32_e32 v38, v12, v4
	v_lshlrev_b32_e32 v4, 16, v5
	v_fmac_f32_e32 v39, v12, v4
	v_and_b32_e32 v4, 0xffff0000, v5
	v_sub_f32_e32 v5, v31, v36
	v_fmac_f32_e32 v40, v12, v4
	v_lshlrev_b32_e32 v4, 16, v6
	v_mul_f32_e32 v5, 0x3e38aa3b, v5
	v_fmac_f32_e32 v16, v12, v15
	v_fmac_f32_e32 v41, v12, v4
	v_and_b32_e32 v4, 0xffff0000, v6
	v_exp_f32_e32 v15, v5
	v_fmac_f32_e32 v42, v12, v4
	v_lshlrev_b32_e32 v4, 16, v7
	v_fmac_f32_e32 v43, v12, v4
	v_and_b32_e32 v4, 0xffff0000, v7
	v_fmac_f32_e32 v37, v12, v4
	s_waitcnt lgkmcnt(0)
	v_lshlrev_b32_e32 v4, 16, v8
	v_fmac_f32_e32 v16, v15, v4
	v_and_b32_e32 v4, 0xffff0000, v8
	v_fmac_f32_e32 v38, v15, v4
	v_lshlrev_b32_e32 v4, 16, v9
	v_fmac_f32_e32 v39, v15, v4
	v_and_b32_e32 v4, 0xffff0000, v9
	v_fmac_f32_e32 v40, v15, v4
	v_lshlrev_b32_e32 v4, 16, v10
	v_fmac_f32_e32 v41, v15, v4
	v_and_b32_e32 v4, 0xffff0000, v10
	v_fmac_f32_e32 v42, v15, v4
	v_lshlrev_b32_e32 v4, 16, v11
	v_fmac_f32_e32 v43, v15, v4
	v_sub_f32_e32 v4, v33, v36
	v_mul_f32_e32 v4, 0x3e38aa3b, v4
	v_exp_f32_e32 v12, v4
	ds_read_b128 v[4:7], v14 offset:49152
	v_and_b32_e32 v8, 0xffff0000, v11
	v_fmac_f32_e32 v37, v15, v8
	ds_read_b128 v[8:11], v14 offset:57344
	v_fmac_f32_e32 v13, v32, v15
	s_waitcnt lgkmcnt(1)
	v_lshlrev_b32_e32 v14, 16, v4
	v_and_b32_e32 v4, 0xffff0000, v4
	v_fmac_f32_e32 v38, v12, v4
	v_lshlrev_b32_e32 v4, 16, v5
	v_fmac_f32_e32 v39, v12, v4
	v_and_b32_e32 v4, 0xffff0000, v5
	v_sub_f32_e32 v5, v28, v36
	v_fmac_f32_e32 v40, v12, v4
	v_lshlrev_b32_e32 v4, 16, v6
	v_mul_f32_e32 v5, 0x3e38aa3b, v5
	v_fmac_f32_e32 v41, v12, v4
	v_and_b32_e32 v4, 0xffff0000, v6
	v_exp_f32_e32 v5, v5
	v_fmac_f32_e32 v42, v12, v4
	v_lshlrev_b32_e32 v4, 16, v7
	v_fmac_f32_e32 v43, v12, v4
	v_and_b32_e32 v4, 0xffff0000, v7
	v_fmac_f32_e32 v16, v12, v14
	v_fmac_f32_e32 v37, v12, v4
	s_waitcnt lgkmcnt(0)
	v_lshlrev_b32_e32 v4, 16, v8
	v_fmac_f32_e32 v16, v5, v4
	v_and_b32_e32 v4, 0xffff0000, v8
	v_fmac_f32_e32 v38, v5, v4
	v_lshlrev_b32_e32 v4, 16, v9
	v_fmac_f32_e32 v13, v34, v12
	v_fmac_f32_e32 v39, v5, v4
	v_and_b32_e32 v4, 0xffff0000, v9
	v_fmac_f32_e32 v13, v35, v5
	v_fmac_f32_e32 v40, v5, v4
	v_lshlrev_b32_e32 v4, 16, v10
	v_fmac_f32_e32 v41, v5, v4
	v_and_b32_e32 v4, 0xffff0000, v10
	v_rcp_f32_e32 v6, v13
	v_fmac_f32_e32 v42, v5, v4
	v_lshlrev_b32_e32 v4, 16, v11
	v_fmac_f32_e32 v43, v5, v4
	v_and_b32_e32 v4, 0xffff0000, v11
	v_fmac_f32_e32 v37, v5, v4
	s_waitcnt vmcnt(32)
	v_fmac_f32_e32 v111, v6, v38
	v_fmac_f32_e32 v112, v6, v39
	global_store_dword v118, v111, s[80:81] offset:-4096 nt
	global_store_dword v118, v112, s[80:81] nt
	v_fmac_f32_e32 v117, v6, v40
	global_store_dword v118, v117, s[82:83] nt
	v_fmac_f32_e32 v113, v6, v41
	global_store_dword v118, v113, s[84:85] offset:-4096 nt
	v_fmac_f32_e32 v114, v6, v42
	global_store_dword v118, v114, s[84:85] nt
	v_fmac_f32_e32 v110, v6, v16
	global_store_dword v118, v110, s[14:15] nt
	v_fmac_f32_e32 v115, v6, v43
	v_fmac_f32_e32 v116, v6, v37
	s_and_b64 vcc, exec, s[18:19]
	global_store_dword v118, v115, s[86:87] offset:-4096 nt
	global_store_dword v118, v116, s[86:87] nt
	s_barrier
	s_cbranch_vccnz .LBB3_144
